# stack20 = stack19 + grid barriers: two poll loads kept in flight (counter sampled twice per memory round trip)
# baseline (speedup 1.0000x reference)
; DEVINL unsigned xb_ld(unsigned* p)              { return __hip_atomic_load(p, __ATOMIC_RELAXED, __HIP_MEMORY_SCOPE_AGENT); }
; #define XB_SPIN(cond, bar) do { unsigned _sp = 0; while (cond) { __builtin_amdgcn_s_sleep(1); \
;     if ((++_sp & 255u) == 0u) { if (xb_ld(&(bar)[XB_TMO])) break; if (_sp > XB_SPIN_CAP) { atomicAdd(&(bar)[XB_TMO], 1u); break; } } } } while (0)
; DEVINL void stage_x_load(const Params& P, int m0, XPre& X) {
;     const int wv = __builtin_amdgcn_readfirstlane(threadIdx.x >> 6); int lane = threadIdx.x & 63; asm volatile("" : "+v"(lane));
; #pragma unroll
;     for (int rr = 0; rr < 8; ++rr) {
;         const f32x4* xr = (const f32x4*)(P.x + (size_t)(m0 + 8 * wv + rr) * DM) + lane;
; #pragma unroll
;         for (int j = 0; j < 4; ++j) X.v[rr][j] = __builtin_nontemporal_load(xr + 64 * j);
;     }
; template <int W> DEVINL void xcd_barrier_w(const XcdBarrier& b, const Params& P, XPre& X) {
;     ...
;         XB_SPIN(xb_ld(&bar[XB_TOPI((W - 1))]) < nx, bar);
.LBB0_154:
	s_or_b64 exec, exec, s[4:5]
	buffer_inv sc1
	s_mov_b64 s[12:13], exec
	s_mov_b64 exec, -1
	s_load_dwordx2 s[14:15], s[96:97], 0x0
	v_and_b32_e32 v2, 63, v0
	s_lshl_b32 s16, s80, 18
	v_lshlrev_b32_e32 v2, 4, v2
	s_waitcnt lgkmcnt(0)
	s_add_u32 s14, s14, s16
	s_addc_u32 s15, s15, 0
	global_load_dwordx4 v[126:129], v2, s[14:15] nt
	global_load_dwordx4 v[122:125], v2, s[14:15] offset:1024 nt
	global_load_dwordx4 v[118:121], v2, s[14:15] offset:2048 nt
	global_load_dwordx4 v[114:117], v2, s[14:15] offset:3072 nt
	s_add_u32 s14, s14, 0x1000
	s_addc_u32 s15, s15, 0
	global_load_dwordx4 v[110:113], v2, s[14:15] nt
	global_load_dwordx4 v[106:109], v2, s[14:15] offset:1024 nt
	global_load_dwordx4 v[102:105], v2, s[14:15] offset:2048 nt
	global_load_dwordx4 v[98:101], v2, s[14:15] offset:3072 nt
	s_add_u32 s14, s14, 0x1000
	s_addc_u32 s15, s15, 0
	global_load_dwordx4 v[94:97], v2, s[14:15] nt
	global_load_dwordx4 v[90:93], v2, s[14:15] offset:1024 nt
	global_load_dwordx4 v[86:89], v2, s[14:15] offset:2048 nt
	global_load_dwordx4 v[82:85], v2, s[14:15] offset:3072 nt
	s_add_u32 s14, s14, 0x1000
	s_addc_u32 s15, s15, 0
	global_load_dwordx4 v[78:81], v2, s[14:15] nt
	global_load_dwordx4 v[74:77], v2, s[14:15] offset:1024 nt
	global_load_dwordx4 v[70:73], v2, s[14:15] offset:2048 nt
	global_load_dwordx4 v[66:69], v2, s[14:15] offset:3072 nt
	s_add_u32 s14, s14, 0x1000
	s_addc_u32 s15, s15, 0
	global_load_dwordx4 v[62:65], v2, s[14:15] nt
	global_load_dwordx4 v[58:61], v2, s[14:15] offset:1024 nt
	global_load_dwordx4 v[54:57], v2, s[14:15] offset:2048 nt
	global_load_dwordx4 v[50:53], v2, s[14:15] offset:3072 nt
	s_add_u32 s14, s14, 0x1000
	s_addc_u32 s15, s15, 0
	global_load_dwordx4 v[46:49], v2, s[14:15] nt
	global_load_dwordx4 v[42:45], v2, s[14:15] offset:1024 nt
	global_load_dwordx4 v[38:41], v2, s[14:15] offset:2048 nt
	global_load_dwordx4 v[34:37], v2, s[14:15] offset:3072 nt
	s_add_u32 s14, s14, 0x1000
	s_addc_u32 s15, s15, 0
	global_load_dwordx4 v[30:33], v2, s[14:15] nt
	global_load_dwordx4 v[22:25], v2, s[14:15] offset:1024 nt
	global_load_dwordx4 v[18:21], v2, s[14:15] offset:2048 nt
	global_load_dwordx4 v[10:13], v2, s[14:15] offset:3072 nt
	s_add_u32 s14, s14, 0x1000
	s_addc_u32 s15, s15, 0
	global_load_dwordx4 v[26:29], v2, s[14:15] nt
	global_load_dwordx4 v[14:17], v2, s[14:15] offset:1024 nt
	global_load_dwordx4 v[6:9], v2, s[14:15] offset:2048 nt
	global_load_dwordx4 v[2:5], v2, s[14:15] offset:3072 nt
	s_mov_b64 exec, s[12:13]
	v_mov_b32_e32 v1, 0
	s_getpc_b64 s[2:3]
	s_add_u32 s2, s2, g_xbar@rel32@lo+32772
	s_addc_u32 s3, s3, g_xbar@rel32@hi+32780
	global_load_dword v131, v1, s[2:3] sc1
	s_waitcnt vmcnt(0) lgkmcnt(0)
	v_cmp_ge_u32_e32 vcc, v131, v130
	s_cbranch_vccnz .LBB0_167
	global_load_dword v131, v1, s[2:3] sc1
	s_sleep 2
	global_load_dword v132, v1, s[2:3] sc1
	s_mov_b32 s2, 1
	s_branch .LBB0_157

; DEVINL unsigned xb_ld(unsigned* p)              { return __hip_atomic_load(p, __ATOMIC_RELAXED, __HIP_MEMORY_SCOPE_AGENT); }
; #define XB_SPIN(cond, bar) do { unsigned _sp = 0; while (cond) { __builtin_amdgcn_s_sleep(1); \
;     if ((++_sp & 255u) == 0u) { if (xb_ld(&(bar)[XB_TMO])) break; if (_sp > XB_SPIN_CAP) { atomicAdd(&(bar)[XB_TMO], 1u); break; } } } } while (0)
; template <int W> DEVINL void xcd_barrier_w(const XcdBarrier& b, const Params& P, XPre& X) {
;     ...
;         XB_SPIN(xb_ld(&bar[XB_TOPI((W - 1))]) < nx, bar);
.LBB0_159:
	s_getpc_b64 s[4:5]
	s_add_u32 s4, s4, g_xbar@rel32@lo+32772
	s_addc_u32 s5, s5, g_xbar@rel32@hi+32780
	s_add_i32 s2, s2, 1
	s_mov_b64 s[6:7], -1
	s_waitcnt vmcnt(1)
	v_cmp_ge_u32_e32 vcc, v131, v130
	s_cbranch_vccnz .Lpoll_hit0
	global_load_dword v131, v1, s[4:5] sc1
	s_sleep 2
	s_waitcnt vmcnt(1)
	v_cmp_ge_u32_e32 vcc, v132, v130
	s_cbranch_vccnz .Lpoll_hit0
	global_load_dword v132, v1, s[4:5] sc1
	s_mov_b64 s[4:5], 0
	s_branch .LBB0_156
.Lpoll_hit0:
	s_mov_b64 s[4:5], exec
	s_branch .LBB0_156

; DEVINL unsigned xb_ld(unsigned* p)              { return __hip_atomic_load(p, __ATOMIC_RELAXED, __HIP_MEMORY_SCOPE_AGENT); }
; #define XB_SPIN(cond, bar) do { unsigned _sp = 0; while (cond) { __builtin_amdgcn_s_sleep(1); \
;     if ((++_sp & 255u) == 0u) { if (xb_ld(&(bar)[XB_TMO])) break; if (_sp > XB_SPIN_CAP) { atomicAdd(&(bar)[XB_TMO], 1u); break; } } } } while (0)
; template <int W> DEVINL void xcd_barrier_w(const XcdBarrier& b, const Params& P, XPre& X) {
;     ...
;         XB_SPIN(xb_ld(&bar[XB_TOPI((W - 1))]) < nx, bar);
.LBB0_428:
	s_or_b64 exec, exec, s[4:5]
	buffer_inv sc1
	v_mov_b32_e32 v1, 0
	s_getpc_b64 s[2:3]
	s_add_u32 s2, s2, g_xbar@rel32@lo+33028
	s_addc_u32 s3, s3, g_xbar@rel32@hi+33036
	global_load_dword v3, v1, s[2:3] sc1
	s_waitcnt vmcnt(0) lgkmcnt(0)
	v_cmp_ge_u32_e32 vcc, v3, v2
	s_cbranch_vccnz .LBB0_441
	global_load_dword v3, v1, s[2:3] sc1
	s_sleep 2
	global_load_dword v4, v1, s[2:3] sc1
	s_mov_b32 s2, 1
	s_branch .LBB0_431

; DEVINL unsigned xb_ld(unsigned* p)              { return __hip_atomic_load(p, __ATOMIC_RELAXED, __HIP_MEMORY_SCOPE_AGENT); }
; #define XB_SPIN(cond, bar) do { unsigned _sp = 0; while (cond) { __builtin_amdgcn_s_sleep(1); \
;     if ((++_sp & 255u) == 0u) { if (xb_ld(&(bar)[XB_TMO])) break; if (_sp > XB_SPIN_CAP) { atomicAdd(&(bar)[XB_TMO], 1u); break; } } } } while (0)
; template <int W> DEVINL void xcd_barrier_w(const XcdBarrier& b, const Params& P, XPre& X) {
;     ...
;         XB_SPIN(xb_ld(&bar[XB_TOPI((W - 1))]) < nx, bar);
.LBB0_433:
	s_getpc_b64 s[4:5]
	s_add_u32 s4, s4, g_xbar@rel32@lo+33028
	s_addc_u32 s5, s5, g_xbar@rel32@hi+33036
	s_add_i32 s2, s2, 1
	s_mov_b64 s[6:7], -1
	s_waitcnt vmcnt(1)
	v_cmp_ge_u32_e32 vcc, v3, v2
	s_cbranch_vccnz .Lpoll_hit1
	global_load_dword v3, v1, s[4:5] sc1
	s_sleep 2
	s_waitcnt vmcnt(1)
	v_cmp_ge_u32_e32 vcc, v4, v2
	s_cbranch_vccnz .Lpoll_hit1
	global_load_dword v4, v1, s[4:5] sc1
	s_mov_b64 s[4:5], 0
	s_branch .LBB0_430

; DEVINL unsigned xb_ld(unsigned* p)              { return __hip_atomic_load(p, __ATOMIC_RELAXED, __HIP_MEMORY_SCOPE_AGENT); }
; #define XB_SPIN(cond, bar) do { unsigned _sp = 0; while (cond) { __builtin_amdgcn_s_sleep(1); \
;     if ((++_sp & 255u) == 0u) { if (xb_ld(&(bar)[XB_TMO])) break; if (_sp > XB_SPIN_CAP) { atomicAdd(&(bar)[XB_TMO], 1u); break; } } } } while (0)
; template <int W> DEVINL void xcd_barrier_w(const XcdBarrier& b, const Params& P, XPre& X) {
;     ...
;         XB_SPIN(xb_ld(&bar[XB_TOPI((W - 1))]) < nx, bar);
.LBB0_557:
	s_or_b64 exec, exec, s[4:5]
	buffer_inv sc1
	v_mov_b32_e32 v1, 0
	s_getpc_b64 s[2:3]
	s_add_u32 s2, s2, g_xbar@rel32@lo+33284
	s_addc_u32 s3, s3, g_xbar@rel32@hi+33292
	global_load_dword v3, v1, s[2:3] sc1
	s_waitcnt vmcnt(0) lgkmcnt(0)
	v_cmp_ge_u32_e32 vcc, v3, v2
	s_cbranch_vccnz .LBB0_570
	global_load_dword v3, v1, s[2:3] sc1
	s_sleep 2
	global_load_dword v4, v1, s[2:3] sc1
	s_mov_b32 s2, 1
	s_branch .LBB0_560

; DEVINL unsigned xb_ld(unsigned* p)              { return __hip_atomic_load(p, __ATOMIC_RELAXED, __HIP_MEMORY_SCOPE_AGENT); }
; #define XB_SPIN(cond, bar) do { unsigned _sp = 0; while (cond) { __builtin_amdgcn_s_sleep(1); \
;     if ((++_sp & 255u) == 0u) { if (xb_ld(&(bar)[XB_TMO])) break; if (_sp > XB_SPIN_CAP) { atomicAdd(&(bar)[XB_TMO], 1u); break; } } } } while (0)
; template <int W> DEVINL void xcd_barrier_w(const XcdBarrier& b, const Params& P, XPre& X) {
;     ...
;         XB_SPIN(xb_ld(&bar[XB_TOPI((W - 1))]) < nx, bar);
.LBB0_562:
	s_getpc_b64 s[4:5]
	s_add_u32 s4, s4, g_xbar@rel32@lo+33284
	s_addc_u32 s5, s5, g_xbar@rel32@hi+33292
	s_add_i32 s2, s2, 1
	s_mov_b64 s[6:7], -1
	s_waitcnt vmcnt(1)
	v_cmp_ge_u32_e32 vcc, v3, v2
	s_cbranch_vccnz .Lpoll_hit2
	global_load_dword v3, v1, s[4:5] sc1
	s_sleep 2
	s_waitcnt vmcnt(1)
	v_cmp_ge_u32_e32 vcc, v4, v2
	s_cbranch_vccnz .Lpoll_hit2
	global_load_dword v4, v1, s[4:5] sc1
	s_mov_b64 s[4:5], 0
	s_branch .LBB0_559

; DEVINL unsigned xb_ld(unsigned* p)              { return __hip_atomic_load(p, __ATOMIC_RELAXED, __HIP_MEMORY_SCOPE_AGENT); }
; #define XB_SPIN(cond, bar) do { unsigned _sp = 0; while (cond) { __builtin_amdgcn_s_sleep(1); \
;     if ((++_sp & 255u) == 0u) { if (xb_ld(&(bar)[XB_TMO])) break; if (_sp > XB_SPIN_CAP) { atomicAdd(&(bar)[XB_TMO], 1u); break; } } } } while (0)
; DEVINL void xcd_barrier(const XcdBarrier& b, const int bi) {
;     ...
;         XB_SPIN(xb_ld(&bar[XB_TOPI(bi)]) < nx, bar);
.LBB0_663:
	s_or_b64 exec, exec, s[6:7]
	buffer_inv sc1
	v_mov_b32_e32 v1, 0
	s_getpc_b64 s[2:3]
	s_add_u32 s2, s2, g_xbar@rel32@lo+33540
	s_addc_u32 s3, s3, g_xbar@rel32@hi+33548
	global_load_dword v3, v1, s[2:3] sc1
	s_waitcnt vmcnt(0) lgkmcnt(0)
	v_cmp_ge_u32_e32 vcc, v3, v2
	s_cbranch_vccnz .LBB0_676
	global_load_dword v3, v1, s[2:3] sc1
	s_sleep 2
	global_load_dword v4, v1, s[2:3] sc1
	s_mov_b32 s2, 1
	s_branch .LBB0_666

; DEVINL unsigned xb_ld(unsigned* p)              { return __hip_atomic_load(p, __ATOMIC_RELAXED, __HIP_MEMORY_SCOPE_AGENT); }
; #define XB_SPIN(cond, bar) do { unsigned _sp = 0; while (cond) { __builtin_amdgcn_s_sleep(1); \
;     if ((++_sp & 255u) == 0u) { if (xb_ld(&(bar)[XB_TMO])) break; if (_sp > XB_SPIN_CAP) { atomicAdd(&(bar)[XB_TMO], 1u); break; } } } } while (0)
; DEVINL void xcd_barrier(const XcdBarrier& b, const int bi) {
;     ...
;         XB_SPIN(xb_ld(&bar[XB_TOPI(bi)]) < nx, bar);
.LBB0_668:
	s_getpc_b64 s[6:7]
	s_add_u32 s6, s6, g_xbar@rel32@lo+33540
	s_addc_u32 s7, s7, g_xbar@rel32@hi+33548
	s_add_i32 s2, s2, 1
	s_mov_b64 s[8:9], -1
	s_waitcnt vmcnt(1)
	v_cmp_ge_u32_e32 vcc, v3, v2
	s_cbranch_vccnz .Lpoll_hit3
	global_load_dword v3, v1, s[6:7] sc1
	s_sleep 2
	s_waitcnt vmcnt(1)
	v_cmp_ge_u32_e32 vcc, v4, v2
	s_cbranch_vccnz .Lpoll_hit3
	global_load_dword v4, v1, s[6:7] sc1
	s_mov_b64 s[6:7], 0
	s_branch .LBB0_665
.Lpoll_hit3:
	s_mov_b64 s[6:7], exec
	s_branch .LBB0_665
